# rope epilogue: the 16 merged dwordx4 stores lane-transposed through ds_bpermute (quad of adjacent lanes = one row's 128-B line), deferred one group behind
# speedup vs baseline: 1.0137x; 1.0006x over previous
; #define PG8_ST8(rs, b0, p, v) __builtin_amdgcn_raw_buffer_store_b64(v, rs, (int)((const char*)(p) - (const char*)(b0)), 0, 16)
; __device__ __forceinline__ unsigned cvt_pk_bf16(float lo, float hi) { unsigned r; asm volatile("v_cvt_pk_bf16_f32 %0, %1, %2" : "=v"(r) : "v"(lo), "v"(hi)); return r; }
;     __device__ __forceinline__ void operator()(const f32x4 (&acc)[2][2][4][2], const Unit& u, int wr, int wc, int fr, int fq) const {
;     ...
;             const float sc = (pn <= 6 || (pn >= 9 && pn <= 11)) ? qscale : 1.0f;
;             const int f = 16 * (wc & 1) + 4 * fq, col0 = pn * BM + 64 * (wc >> 1) + f;
; #pragma unroll
;             for (int ai = 0; ai < 2; ++ai) {
;                 f32x4 c4[4], s4[4];
; #pragma unroll
;                 for (int m = 0; m < 4; ++m) { const int row = row0 + ai * HALF + m * 16; c4[m] = *(const f32x4*)(rc + (size_t)row * 32 + f); s4[m] = *(const f32x4*)(rs + (size_t)row * 32 + f); }
;                 asm volatile("" ::: "memory");
; #pragma unroll
;                 for (int m = 0; m < 4; ++m) { const int row = row0 + ai * HALF + m * 16;
;                     const f32x4 cc = c4[m] * sc, ss = s4[m] * sc;
;                     bf16_t* rowp = P + (size_t)row * ldp + col0;
; #pragma unroll
;                     for (int bj = 0; bj < 2; ++bj) { const f32x4 x1 = acc[ai][bj][m][0], x2 = acc[ai][bj][m][1]; const f32x4 o1 = x1 * cc - x2 * ss, o2 = x2 * cc + x1 * ss;
;                         u32x2 w1, w2; w1.x = cvt_pk_bf16(o1[0], o1[1]); w1.y = cvt_pk_bf16(o1[2], o1[3]); w2.x = cvt_pk_bf16(o2[0], o2[1]); w2.y = cvt_pk_bf16(o2[2], o2[3]);
;                         PG8_ST8(rsp_, P, rowp + bj * HALF, w1); PG8_ST8(rsp_, P, rowp + bj * HALF + 32, w2); } }
.LBB0_230:
	v_lshl_add_u32 v164, s27, 8, v175
	s_add_i32 s27, s62, s56
	s_cmp_gt_i32 s27, 3
	s_mov_b64 s[34:35], -1
	s_cbranch_scc0 .LBB0_237
	s_cmp_lg_u32 s27, 8
	s_cselect_b64 s[34:35], -1, 0
	s_cmp_lt_u32 s27, 15
	s_cselect_b64 s[36:37], -1, 0
	s_and_b64 s[36:37], s[34:35], s[36:37]
	s_mov_b64 s[34:35], -1
	s_and_b64 vcc, exec, s[36:37]
	v_add_u32_e32 v172, 0x80, v164
	v_add_u32_e32 v170, 0x90, v164
	v_add_u32_e32 v168, 0xa0, v164
	v_add_u32_e32 v166, 0xb0, v164
	s_cbranch_vccz .LBB0_233
	s_cmp_lt_u32 s27, 7
	s_cselect_b64 s[34:35], -1, 0
	s_add_i32 s36, s27, -9
	s_cmp_lt_u32 s36, 3
	s_cselect_b64 s[36:37], -1, 0
	s_or_b64 vcc, s[34:35], s[36:37]
	v_mov_b32_e32 v132, 0x3e38aa3b
	v_ashrrev_i32_e32 v165, 31, v164
	v_cndmask_b32_e32 v174, 1.0, v132, vcc
	v_lshlrev_b64 v[132:133], 7, v[164:165]
	v_lshl_add_u64 v[134:135], v[154:155], 0, v[132:133]
	v_lshl_add_u64 v[132:133], v[156:157], 0, v[132:133]
	global_load_dwordx4 v[176:179], v[134:135], off
	global_load_dwordx4 v[184:187], v[132:133], off
	v_or_b32_e32 v192, 16, v164
	v_ashrrev_i32_e32 v193, 31, v192
	v_lshlrev_b64 v[132:133], 7, v[192:193]
	v_lshl_add_u64 v[134:135], v[154:155], 0, v[132:133]
	v_lshl_add_u64 v[132:133], v[156:157], 0, v[132:133]
	global_load_dwordx4 v[188:191], v[134:135], off
	global_load_dwordx4 v[218:221], v[132:133], off
	v_or_b32_e32 v182, 32, v164
	v_ashrrev_i32_e32 v183, 31, v182
	v_lshlrev_b64 v[132:133], 7, v[182:183]
	v_lshl_add_u64 v[134:135], v[154:155], 0, v[132:133]
	v_lshl_add_u64 v[132:133], v[156:157], 0, v[132:133]
	global_load_dwordx4 v[144:147], v[134:135], off
	global_load_dwordx4 v[140:143], v[132:133], off
	v_or_b32_e32 v180, 48, v164
	v_ashrrev_i32_e32 v181, 31, v180
	v_lshlrev_b64 v[132:133], 7, v[180:181]
	v_lshl_add_u64 v[134:135], v[154:155], 0, v[132:133]
	v_lshl_add_u64 v[132:133], v[156:157], 0, v[132:133]
	global_load_dwordx4 v[136:139], v[134:135], off
	s_movk_i32 s36, 0x2400
	global_load_dwordx4 v[132:135], v[132:133], off
	v_ashrrev_i32_e32 v173, 31, v172
	v_ashrrev_i32_e32 v171, 31, v170
	v_ashrrev_i32_e32 v169, 31, v168
	v_ashrrev_i32_e32 v167, 31, v166
	s_waitcnt vmcnt(0)
	v_pk_mul_f32 v[198:199], v[174:175], v[178:179] op_sel_hi:[0,1]
	v_pk_mul_f32 v[186:187], v[174:175], v[186:187] op_sel_hi:[0,1]
	v_pk_mul_f32 v[184:185], v[174:175], v[184:185] op_sel_hi:[0,1]
	v_pk_mul_f32 v[200:201], v[174:175], v[176:177] op_sel_hi:[0,1]
	v_mov_b64_e32 v[176:177], s[20:21]
	v_lshrrev_b32_e32 v245, 2, v215
	v_and_b32_e32 v246, 15, v215
	v_sub_u32_e32 v245, v245, v246
	v_mad_i64_i32 v[176:177], s[34:35], v245, s36, v[176:177]
	v_pk_mul_f32 v[208:209], v[118:119], v[186:187]
	v_pk_mul_f32 v[222:223], v[116:117], v[184:185]
	v_mad_i64_i32 v[206:207], s[34:35], v164, s36, v[176:177]
	v_lshl_or_b32 v178, s27, 9, v202
	v_mov_b32_e32 v179, v2
	v_and_b32_e32 v244, 3, v215
	v_lshrrev_b32_e32 v246, 4, v215
	v_sub_u32_e32 v246, v244, v246
	v_lshl_add_u32 v178, v246, 3, v178
	v_and_b32_e32 v246, 1, v215
	v_mad_u32_u24 v178, v246, 56, v178
	v_and_b32_e32 v246, 60, v215
	v_lshl_or_b32 v244, v244, 6, v246
	v_pk_fma_f32 v[208:209], v[126:127], v[198:199], v[208:209] neg_lo:[0,0,1] neg_hi:[0,0,1]
	v_pk_fma_f32 v[222:223], v[124:125], v[200:201], v[222:223] neg_lo:[0,0,1] neg_hi:[0,0,1]
	v_pk_mul_f32 v[224:225], v[126:127], v[186:187]
	v_pk_mul_f32 v[226:227], v[124:125], v[184:185]
	v_lshl_add_u64 v[206:207], v[206:207], 0, v[178:179]
	v_pk_fma_f32 v[224:225], v[118:119], v[198:199], v[224:225]
	v_pk_fma_f32 v[226:227], v[116:117], v[200:201], v[226:227]
	v_cvt_pk_bf16_f32 v222, v222, v223
	v_cvt_pk_bf16_f32 v223, v208, v209
	v_mad_i64_i32 v[192:193], s[34:35], v192, s36, v[176:177]
	v_cvt_pk_bf16_f32 v208, v226, v227
	v_cvt_pk_bf16_f32 v209, v224, v225
	v_mov_b32_e32 v228, v222
	v_mov_b32_e32 v229, v223
	v_mov_b32_e32 v230, v208
	v_mov_b32_e32 v231, v209
	s_nop 1
	v_permlane16_swap_b32_e32 v228, v230
	v_permlane16_swap_b32_e32 v229, v231
	ds_bpermute_b32 v228, v244, v228
	ds_bpermute_b32 v229, v244, v229
	ds_bpermute_b32 v230, v244, v230
	ds_bpermute_b32 v231, v244, v231
	v_pk_mul_f32 v[208:209], v[122:123], v[186:187]
	v_pk_mul_f32 v[222:223], v[120:121], v[184:185]
	v_pk_mul_f32 v[186:187], v[130:131], v[186:187]
	v_pk_mul_f32 v[184:185], v[128:129], v[184:185]
	v_pk_fma_f32 v[186:187], v[122:123], v[198:199], v[186:187]
	v_pk_fma_f32 v[184:185], v[120:121], v[200:201], v[184:185]
	v_pk_fma_f32 v[208:209], v[130:131], v[198:199], v[208:209] neg_lo:[0,0,1] neg_hi:[0,0,1]
	v_pk_fma_f32 v[222:223], v[128:129], v[200:201], v[222:223] neg_lo:[0,0,1] neg_hi:[0,0,1]
	v_lshl_add_u64 v[192:193], v[192:193], 0, v[178:179]
	v_cvt_pk_bf16_f32 v198, v222, v223
	v_cvt_pk_bf16_f32 v199, v208, v209
	v_cvt_pk_bf16_f32 v184, v184, v185
	v_cvt_pk_bf16_f32 v185, v186, v187
	v_pk_mul_f32 v[186:187], v[174:175], v[190:191] op_sel_hi:[0,1]
	v_pk_mul_f32 v[190:191], v[174:175], v[218:219] op_sel_hi:[0,1]
	v_mov_b32_e32 v232, v198
	v_mov_b32_e32 v233, v199
	v_mov_b32_e32 v234, v184
	v_mov_b32_e32 v235, v185
	s_nop 1
	v_permlane16_swap_b32_e32 v232, v234
	v_permlane16_swap_b32_e32 v233, v235
	ds_bpermute_b32 v232, v244, v232
	ds_bpermute_b32 v233, v244, v233
	ds_bpermute_b32 v234, v244, v234
	ds_bpermute_b32 v235, v244, v235
	s_waitcnt lgkmcnt(4)
; #define PG8_ST8(rs, b0, p, v) __builtin_amdgcn_raw_buffer_store_b64(v, rs, (int)((const char*)(p) - (const char*)(b0)), 0, 16)
; __device__ __forceinline__ unsigned cvt_pk_bf16(float lo, float hi) { unsigned r; asm volatile("v_cvt_pk_bf16_f32 %0, %1, %2" : "=v"(r) : "v"(lo), "v"(hi)); return r; }
;     __device__ __forceinline__ void operator()(const f32x4 (&acc)[2][2][4][2], const Unit& u, int wr, int wc, int fr, int fq) const {
;     ...
;                 for (int m = 0; m < 4; ++m) { const int row = row0 + ai * HALF + m * 16;
;                     const f32x4 cc = c4[m] * sc, ss = s4[m] * sc;
;                     bf16_t* rowp = P + (size_t)row * ldp + col0;
; #pragma unroll
;                     for (int bj = 0; bj < 2; ++bj) { const f32x4 x1 = acc[ai][bj][m][0], x2 = acc[ai][bj][m][1]; const f32x4 o1 = x1 * cc - x2 * ss, o2 = x2 * cc + x1 * ss;
;                         u32x2 w1, w2; w1.x = cvt_pk_bf16(o1[0], o1[1]); w1.y = cvt_pk_bf16(o1[2], o1[3]); w2.x = cvt_pk_bf16(o2[0], o2[1]); w2.y = cvt_pk_bf16(o2[2], o2[3]);
;                         PG8_ST8(rsp_, P, rowp + bj * HALF, w1); PG8_ST8(rsp_, P, rowp + bj * HALF + 32, w2); } }
	global_store_dwordx4 v[206:207], v[228:231], off
	v_pk_mul_f32 v[184:185], v[174:175], v[188:189] op_sel_hi:[0,1]
	v_pk_mul_f32 v[188:189], v[174:175], v[220:221] op_sel_hi:[0,1]
	v_pk_mul_f32 v[198:199], v[100:101], v[190:191]
	v_pk_mul_f32 v[200:201], v[102:103], v[188:189]
	v_pk_fma_f32 v[198:199], v[108:109], v[184:185], v[198:199] neg_lo:[0,0,1] neg_hi:[0,0,1]
	v_pk_fma_f32 v[200:201], v[110:111], v[186:187], v[200:201] neg_lo:[0,0,1] neg_hi:[0,0,1]
	v_pk_mul_f32 v[204:205], v[108:109], v[190:191]
	v_pk_mul_f32 v[208:209], v[110:111], v[188:189]
	v_cvt_pk_bf16_f32 v198, v198, v199
	v_cvt_pk_bf16_f32 v199, v200, v201
	v_pk_fma_f32 v[204:205], v[100:101], v[184:185], v[204:205]
	v_pk_fma_f32 v[208:209], v[102:103], v[186:187], v[208:209]
	v_cvt_pk_bf16_f32 v200, v204, v205
	v_pk_mul_f32 v[142:143], v[174:175], v[142:143] op_sel_hi:[0,1]
	v_cvt_pk_bf16_f32 v201, v208, v209
	v_mov_b32_e32 v236, v198
	v_mov_b32_e32 v237, v199
	v_mov_b32_e32 v238, v200
	v_mov_b32_e32 v239, v201
	s_nop 1
	v_permlane16_swap_b32_e32 v236, v238
	v_permlane16_swap_b32_e32 v237, v239
	ds_bpermute_b32 v236, v244, v236
	ds_bpermute_b32 v237, v244, v237
	ds_bpermute_b32 v238, v244, v238
	ds_bpermute_b32 v239, v244, v239
	s_waitcnt lgkmcnt(4)
	global_store_dwordx4 v[206:207], v[232:235], off offset:256
	v_pk_mul_f32 v[198:199], v[104:105], v[190:191]
	v_pk_mul_f32 v[190:191], v[112:113], v[190:191]
	v_pk_mul_f32 v[200:201], v[106:107], v[188:189]
	v_pk_fma_f32 v[198:199], v[112:113], v[184:185], v[198:199] neg_lo:[0,0,1] neg_hi:[0,0,1]
	v_pk_mul_f32 v[188:189], v[114:115], v[188:189]
	v_pk_fma_f32 v[184:185], v[104:105], v[184:185], v[190:191]
	v_pk_fma_f32 v[200:201], v[114:115], v[186:187], v[200:201] neg_lo:[0,0,1] neg_hi:[0,0,1]
	v_pk_fma_f32 v[186:187], v[106:107], v[186:187], v[188:189]
	v_cvt_pk_bf16_f32 v188, v198, v199
	v_cvt_pk_bf16_f32 v189, v200, v201
	v_cvt_pk_bf16_f32 v184, v184, v185
	v_pk_mul_f32 v[140:141], v[174:175], v[140:141] op_sel_hi:[0,1]
	v_cvt_pk_bf16_f32 v185, v186, v187
	v_mov_b32_e32 v240, v188
	v_mov_b32_e32 v241, v189
	v_mov_b32_e32 v242, v184
	v_mov_b32_e32 v243, v185
	s_nop 1
	v_permlane16_swap_b32_e32 v240, v242
	v_permlane16_swap_b32_e32 v241, v243
	ds_bpermute_b32 v240, v244, v240
	ds_bpermute_b32 v241, v244, v241
	ds_bpermute_b32 v242, v244, v242
	ds_bpermute_b32 v243, v244, v243
	s_waitcnt lgkmcnt(4)
	global_store_dwordx4 v[192:193], v[236:239], off
	v_pk_mul_f32 v[144:145], v[174:175], v[144:145] op_sel_hi:[0,1]
	v_pk_mul_f32 v[146:147], v[174:175], v[146:147] op_sel_hi:[0,1]
	v_pk_mul_f32 v[184:185], v[84:85], v[140:141]
	v_pk_mul_f32 v[186:187], v[86:87], v[142:143]
	v_mad_i64_i32 v[182:183], s[34:35], v182, s36, v[176:177]
	v_pk_fma_f32 v[186:187], v[94:95], v[146:147], v[186:187] neg_lo:[0,0,1] neg_hi:[0,0,1]
	v_pk_fma_f32 v[184:185], v[92:93], v[144:145], v[184:185] neg_lo:[0,0,1] neg_hi:[0,0,1]
	v_pk_mul_f32 v[188:189], v[92:93], v[140:141]
	v_pk_mul_f32 v[190:191], v[94:95], v[142:143]
	v_lshl_add_u64 v[182:183], v[182:183], 0, v[178:179]
	v_pk_fma_f32 v[190:191], v[86:87], v[146:147], v[190:191]
	v_pk_fma_f32 v[188:189], v[84:85], v[144:145], v[188:189]
	v_cvt_pk_bf16_f32 v184, v184, v185
	v_cvt_pk_bf16_f32 v185, v186, v187
	v_pk_mul_f32 v[134:135], v[174:175], v[134:135] op_sel_hi:[0,1]
	v_cvt_pk_bf16_f32 v186, v188, v189
	v_cvt_pk_bf16_f32 v187, v190, v191
	v_mov_b32_e32 v228, v184
	v_mov_b32_e32 v229, v185
	v_mov_b32_e32 v230, v186
	v_mov_b32_e32 v231, v187
	s_nop 1
	v_permlane16_swap_b32_e32 v228, v230
	v_permlane16_swap_b32_e32 v229, v231
	ds_bpermute_b32 v228, v244, v228
	ds_bpermute_b32 v229, v244, v229
	ds_bpermute_b32 v230, v244, v230
	ds_bpermute_b32 v231, v244, v231
	s_waitcnt lgkmcnt(4)
	global_store_dwordx4 v[192:193], v[240:243], off offset:256
	v_pk_mul_f32 v[184:185], v[88:89], v[140:141]
	v_pk_mul_f32 v[186:187], v[90:91], v[142:143]
	v_pk_mul_f32 v[140:141], v[96:97], v[140:141]
	v_pk_mul_f32 v[142:143], v[98:99], v[142:143]
	v_pk_fma_f32 v[186:187], v[98:99], v[146:147], v[186:187] neg_lo:[0,0,1] neg_hi:[0,0,1]
	v_pk_fma_f32 v[184:185], v[96:97], v[144:145], v[184:185] neg_lo:[0,0,1] neg_hi:[0,0,1]
	v_pk_fma_f32 v[142:143], v[90:91], v[146:147], v[142:143]
	v_pk_fma_f32 v[140:141], v[88:89], v[144:145], v[140:141]
	v_cvt_pk_bf16_f32 v144, v184, v185
	v_cvt_pk_bf16_f32 v145, v186, v187
	v_pk_mul_f32 v[132:133], v[174:175], v[132:133] op_sel_hi:[0,1]
	v_cvt_pk_bf16_f32 v140, v140, v141
	v_cvt_pk_bf16_f32 v141, v142, v143
	v_mov_b32_e32 v232, v144
	v_mov_b32_e32 v233, v145
	v_mov_b32_e32 v234, v140
	v_mov_b32_e32 v235, v141
	s_nop 1
	v_permlane16_swap_b32_e32 v232, v234
	v_permlane16_swap_b32_e32 v233, v235
	ds_bpermute_b32 v232, v244, v232
	ds_bpermute_b32 v233, v244, v233
	ds_bpermute_b32 v234, v244, v234
	ds_bpermute_b32 v235, v244, v235
	s_waitcnt lgkmcnt(4)
	global_store_dwordx4 v[182:183], v[228:231], off
	v_pk_mul_f32 v[136:137], v[174:175], v[136:137] op_sel_hi:[0,1]
	v_pk_mul_f32 v[138:139], v[174:175], v[138:139] op_sel_hi:[0,1]
	v_pk_mul_f32 v[142:143], v[68:69], v[132:133]
	v_pk_mul_f32 v[144:145], v[70:71], v[134:135]
	v_mad_i64_i32 v[140:141], s[34:35], v180, s36, v[176:177]
	v_pk_fma_f32 v[144:145], v[78:79], v[138:139], v[144:145] neg_lo:[0,0,1] neg_hi:[0,0,1]
	v_pk_fma_f32 v[142:143], v[76:77], v[136:137], v[142:143] neg_lo:[0,0,1] neg_hi:[0,0,1]
	v_pk_mul_f32 v[146:147], v[76:77], v[132:133]
	v_pk_mul_f32 v[180:181], v[78:79], v[134:135]
	v_lshl_add_u64 v[140:141], v[140:141], 0, v[178:179]
	v_pk_fma_f32 v[180:181], v[70:71], v[138:139], v[180:181]
	v_pk_fma_f32 v[146:147], v[68:69], v[136:137], v[146:147]
	v_cvt_pk_bf16_f32 v142, v142, v143
	v_cvt_pk_bf16_f32 v143, v144, v145
	v_lshlrev_b64 v[184:185], 7, v[168:169]
	v_cvt_pk_bf16_f32 v144, v146, v147
	v_cvt_pk_bf16_f32 v145, v180, v181
	v_mov_b32_e32 v236, v142
	v_mov_b32_e32 v237, v143
	v_mov_b32_e32 v238, v144
	v_mov_b32_e32 v239, v145
	s_nop 1
	v_permlane16_swap_b32_e32 v236, v238
	v_permlane16_swap_b32_e32 v237, v239
	ds_bpermute_b32 v236, v244, v236
	ds_bpermute_b32 v237, v244, v237
	ds_bpermute_b32 v238, v244, v238
	ds_bpermute_b32 v239, v244, v239
	s_waitcnt lgkmcnt(4)
; #define PG8_ST8(rs, b0, p, v) __builtin_amdgcn_raw_buffer_store_b64(v, rs, (int)((const char*)(p) - (const char*)(b0)), 0, 16)
; __device__ __forceinline__ unsigned cvt_pk_bf16(float lo, float hi) { unsigned r; asm volatile("v_cvt_pk_bf16_f32 %0, %1, %2" : "=v"(r) : "v"(lo), "v"(hi)); return r; }
;     __device__ __forceinline__ void operator()(const f32x4 (&acc)[2][2][4][2], const Unit& u, int wr, int wc, int fr, int fq) const {
;     ...
;             for (int ai = 0; ai < 2; ++ai) {
;                 f32x4 c4[4], s4[4];
; #pragma unroll
;                 for (int m = 0; m < 4; ++m) { const int row = row0 + ai * HALF + m * 16; c4[m] = *(const f32x4*)(rc + (size_t)row * 32 + f); s4[m] = *(const f32x4*)(rs + (size_t)row * 32 + f); }
;                 asm volatile("" ::: "memory");
; #pragma unroll
;                 for (int m = 0; m < 4; ++m) { const int row = row0 + ai * HALF + m * 16;
;                     const f32x4 cc = c4[m] * sc, ss = s4[m] * sc;
;                     bf16_t* rowp = P + (size_t)row * ldp + col0;
; #pragma unroll
;                     for (int bj = 0; bj < 2; ++bj) { const f32x4 x1 = acc[ai][bj][m][0], x2 = acc[ai][bj][m][1]; const f32x4 o1 = x1 * cc - x2 * ss, o2 = x2 * cc + x1 * ss;
;                         u32x2 w1, w2; w1.x = cvt_pk_bf16(o1[0], o1[1]); w1.y = cvt_pk_bf16(o1[2], o1[3]); w2.x = cvt_pk_bf16(o2[0], o2[1]); w2.y = cvt_pk_bf16(o2[2], o2[3]);
;                         PG8_ST8(rsp_, P, rowp + bj * HALF, w1); PG8_ST8(rsp_, P, rowp + bj * HALF + 32, w2); } }
	global_store_dwordx4 v[182:183], v[232:235], off offset:256
	v_pk_mul_f32 v[142:143], v[72:73], v[132:133]
	v_pk_mul_f32 v[144:145], v[74:75], v[134:135]
	v_pk_mul_f32 v[132:133], v[80:81], v[132:133]
	v_pk_fma_f32 v[144:145], v[82:83], v[138:139], v[144:145] neg_lo:[0,0,1] neg_hi:[0,0,1]
	v_pk_fma_f32 v[142:143], v[80:81], v[136:137], v[142:143] neg_lo:[0,0,1] neg_hi:[0,0,1]
	v_pk_mul_f32 v[134:135], v[82:83], v[134:135]
	v_pk_fma_f32 v[132:133], v[72:73], v[136:137], v[132:133]
	v_cvt_pk_bf16_f32 v136, v142, v143
	v_cvt_pk_bf16_f32 v137, v144, v145
	v_pk_fma_f32 v[134:135], v[74:75], v[138:139], v[134:135]
	v_cvt_pk_bf16_f32 v132, v132, v133
	v_lshlrev_b64 v[144:145], 7, v[170:171]
	v_cvt_pk_bf16_f32 v133, v134, v135
	v_mov_b32_e32 v240, v136
	v_mov_b32_e32 v241, v137
	v_mov_b32_e32 v242, v132
	v_mov_b32_e32 v243, v133
	s_nop 1
	v_permlane16_swap_b32_e32 v240, v242
	v_permlane16_swap_b32_e32 v241, v243
	ds_bpermute_b32 v240, v244, v240
	ds_bpermute_b32 v241, v244, v241
	ds_bpermute_b32 v242, v244, v242
	ds_bpermute_b32 v243, v244, v243
	s_waitcnt lgkmcnt(4)
	global_store_dwordx4 v[140:141], v[236:239], off
	s_waitcnt lgkmcnt(0)
	global_store_dwordx4 v[140:141], v[240:243], off offset:256
	v_lshlrev_b64 v[136:137], 7, v[172:173]
	v_lshl_add_u64 v[132:133], v[154:155], 0, v[136:137]
	v_lshl_add_u64 v[136:137], v[156:157], 0, v[136:137]
	global_load_dwordx4 v[132:135], v[132:133], off
	v_lshl_add_u64 v[140:141], v[154:155], 0, v[144:145]
	global_load_dwordx4 v[136:139], v[136:137], off
	v_lshl_add_u64 v[144:145], v[156:157], 0, v[144:145]
	global_load_dwordx4 v[140:143], v[140:141], off
	v_lshl_add_u64 v[180:181], v[154:155], 0, v[184:185]
	global_load_dwordx4 v[144:147], v[144:145], off
	v_lshl_add_u64 v[184:185], v[156:157], 0, v[184:185]
	global_load_dwordx4 v[180:183], v[180:181], off
	v_lshlrev_b64 v[192:193], 7, v[166:167]
	global_load_dwordx4 v[184:187], v[184:185], off
	v_lshl_add_u64 v[188:189], v[154:155], 0, v[192:193]
	v_lshl_add_u64 v[192:193], v[156:157], 0, v[192:193]
	global_load_dwordx4 v[188:191], v[188:189], off
	global_load_dwordx4 v[218:221], v[192:193], off
	s_waitcnt vmcnt(0)
	v_pk_mul_f32 v[132:133], v[174:175], v[132:133] op_sel_hi:[0,1]
	v_pk_mul_f32 v[138:139], v[174:175], v[138:139] op_sel_hi:[0,1]
	v_pk_mul_f32 v[136:137], v[174:175], v[136:137] op_sel_hi:[0,1]
	v_pk_mul_f32 v[134:135], v[174:175], v[134:135] op_sel_hi:[0,1]
	v_pk_mul_f32 v[198:199], v[52:53], v[136:137]
	v_pk_mul_f32 v[200:201], v[54:55], v[138:139]
	v_mad_i64_i32 v[206:207], s[34:35], v172, s36, v[176:177]
	v_pk_fma_f32 v[200:201], v[62:63], v[134:135], v[200:201] neg_lo:[0,0,1] neg_hi:[0,0,1]
	v_pk_fma_f32 v[198:199], v[60:61], v[132:133], v[198:199] neg_lo:[0,0,1] neg_hi:[0,0,1]
	v_pk_mul_f32 v[204:205], v[60:61], v[136:137]
	v_pk_mul_f32 v[208:209], v[62:63], v[138:139]
	v_lshl_add_u64 v[206:207], v[206:207], 0, v[178:179]
	v_pk_fma_f32 v[208:209], v[54:55], v[134:135], v[208:209]
	v_pk_fma_f32 v[204:205], v[52:53], v[132:133], v[204:205]
	v_cvt_pk_bf16_f32 v198, v198, v199
	v_cvt_pk_bf16_f32 v199, v200, v201
	s_nop 0
	v_cvt_pk_bf16_f32 v200, v204, v205
	v_cvt_pk_bf16_f32 v201, v208, v209
	v_mov_b32_e32 v228, v198
	v_mov_b32_e32 v229, v199
	v_mov_b32_e32 v230, v200
	v_mov_b32_e32 v231, v201
	s_nop 1
	v_permlane16_swap_b32_e32 v228, v230
	v_permlane16_swap_b32_e32 v229, v231
	ds_bpermute_b32 v228, v244, v228
	ds_bpermute_b32 v229, v244, v229
	ds_bpermute_b32 v230, v244, v230
	ds_bpermute_b32 v231, v244, v231
	v_pk_mul_f32 v[198:199], v[56:57], v[136:137]
	v_pk_mul_f32 v[200:201], v[58:59], v[138:139]
	v_pk_mul_f32 v[136:137], v[64:65], v[136:137]
	v_pk_fma_f32 v[200:201], v[66:67], v[134:135], v[200:201] neg_lo:[0,0,1] neg_hi:[0,0,1]
	v_pk_fma_f32 v[198:199], v[64:65], v[132:133], v[198:199] neg_lo:[0,0,1] neg_hi:[0,0,1]
	v_pk_mul_f32 v[138:139], v[66:67], v[138:139]
	v_pk_fma_f32 v[132:133], v[56:57], v[132:133], v[136:137]
	v_cvt_pk_bf16_f32 v136, v198, v199
	v_cvt_pk_bf16_f32 v137, v200, v201
	v_pk_fma_f32 v[134:135], v[58:59], v[134:135], v[138:139]
	v_cvt_pk_bf16_f32 v132, v132, v133
	v_pk_mul_f32 v[138:139], v[174:175], v[144:145] op_sel_hi:[0,1]
	v_cvt_pk_bf16_f32 v133, v134, v135
	v_mov_b32_e32 v232, v136
	v_mov_b32_e32 v233, v137
	v_mov_b32_e32 v234, v132
	v_mov_b32_e32 v235, v133
	s_nop 1
	v_permlane16_swap_b32_e32 v232, v234
	v_permlane16_swap_b32_e32 v233, v235
	ds_bpermute_b32 v232, v244, v232
	ds_bpermute_b32 v233, v244, v233
	ds_bpermute_b32 v234, v244, v234
	ds_bpermute_b32 v235, v244, v235
	s_waitcnt lgkmcnt(4)
	global_store_dwordx4 v[206:207], v[228:231], off
	v_pk_mul_f32 v[136:137], v[174:175], v[146:147] op_sel_hi:[0,1]
	v_pk_mul_f32 v[132:133], v[174:175], v[140:141] op_sel_hi:[0,1]
	v_pk_mul_f32 v[134:135], v[174:175], v[142:143] op_sel_hi:[0,1]
	v_pk_mul_f32 v[142:143], v[36:37], v[138:139]
	v_pk_mul_f32 v[144:145], v[38:39], v[136:137]
	v_mad_i64_i32 v[140:141], s[34:35], v170, s36, v[176:177]
	v_pk_fma_f32 v[144:145], v[46:47], v[134:135], v[144:145] neg_lo:[0,0,1] neg_hi:[0,0,1]
	v_pk_fma_f32 v[142:143], v[44:45], v[132:133], v[142:143] neg_lo:[0,0,1] neg_hi:[0,0,1]
	v_pk_mul_f32 v[146:147], v[44:45], v[138:139]
	v_pk_mul_f32 v[192:193], v[46:47], v[136:137]
	v_lshl_add_u64 v[140:141], v[140:141], 0, v[178:179]
	v_pk_fma_f32 v[192:193], v[38:39], v[134:135], v[192:193]
	v_pk_fma_f32 v[146:147], v[36:37], v[132:133], v[146:147]
	v_cvt_pk_bf16_f32 v142, v142, v143
	v_cvt_pk_bf16_f32 v143, v144, v145
	s_nop 0
	v_cvt_pk_bf16_f32 v144, v146, v147
	v_cvt_pk_bf16_f32 v145, v192, v193
	v_mov_b32_e32 v236, v142
	v_mov_b32_e32 v237, v143
	v_mov_b32_e32 v238, v144
	v_mov_b32_e32 v239, v145
	s_nop 1
	v_permlane16_swap_b32_e32 v236, v238
	v_permlane16_swap_b32_e32 v237, v239
	ds_bpermute_b32 v236, v244, v236
	ds_bpermute_b32 v237, v244, v237
	ds_bpermute_b32 v238, v244, v238
	ds_bpermute_b32 v239, v244, v239
	s_waitcnt lgkmcnt(4)
; #define PG8_ST8(rs, b0, p, v) __builtin_amdgcn_raw_buffer_store_b64(v, rs, (int)((const char*)(p) - (const char*)(b0)), 0, 16)
; __device__ __forceinline__ unsigned cvt_pk_bf16(float lo, float hi) { unsigned r; asm volatile("v_cvt_pk_bf16_f32 %0, %1, %2" : "=v"(r) : "v"(lo), "v"(hi)); return r; }
;     __device__ __forceinline__ void operator()(const f32x4 (&acc)[2][2][4][2], const Unit& u, int wr, int wc, int fr, int fq) const {
;     ...
;                 for (int m = 0; m < 4; ++m) { const int row = row0 + ai * HALF + m * 16;
;                     const f32x4 cc = c4[m] * sc, ss = s4[m] * sc;
;                     bf16_t* rowp = P + (size_t)row * ldp + col0;
; #pragma unroll
;                     for (int bj = 0; bj < 2; ++bj) { const f32x4 x1 = acc[ai][bj][m][0], x2 = acc[ai][bj][m][1]; const f32x4 o1 = x1 * cc - x2 * ss, o2 = x2 * cc + x1 * ss;
;                         u32x2 w1, w2; w1.x = cvt_pk_bf16(o1[0], o1[1]); w1.y = cvt_pk_bf16(o1[2], o1[3]); w2.x = cvt_pk_bf16(o2[0], o2[1]); w2.y = cvt_pk_bf16(o2[2], o2[3]);
;                         PG8_ST8(rsp_, P, rowp + bj * HALF, w1); PG8_ST8(rsp_, P, rowp + bj * HALF + 32, w2); } }
	global_store_dwordx4 v[206:207], v[232:235], off offset:256
	v_pk_mul_f32 v[142:143], v[40:41], v[138:139]
	v_pk_mul_f32 v[144:145], v[42:43], v[136:137]
	v_pk_mul_f32 v[138:139], v[48:49], v[138:139]
	v_pk_mul_f32 v[136:137], v[50:51], v[136:137]
	v_pk_fma_f32 v[144:145], v[50:51], v[134:135], v[144:145] neg_lo:[0,0,1] neg_hi:[0,0,1]
	v_pk_fma_f32 v[142:143], v[48:49], v[132:133], v[142:143] neg_lo:[0,0,1] neg_hi:[0,0,1]
	v_pk_fma_f32 v[134:135], v[42:43], v[134:135], v[136:137]
	v_pk_fma_f32 v[132:133], v[40:41], v[132:133], v[138:139]
	v_cvt_pk_bf16_f32 v136, v142, v143
	v_cvt_pk_bf16_f32 v137, v144, v145
	v_pk_mul_f32 v[138:139], v[174:175], v[184:185] op_sel_hi:[0,1]
	v_cvt_pk_bf16_f32 v132, v132, v133
	v_cvt_pk_bf16_f32 v133, v134, v135
	v_mov_b32_e32 v240, v136
	v_mov_b32_e32 v241, v137
	v_mov_b32_e32 v242, v132
	v_mov_b32_e32 v243, v133
	s_nop 1
	v_permlane16_swap_b32_e32 v240, v242
	v_permlane16_swap_b32_e32 v241, v243
	ds_bpermute_b32 v240, v244, v240
	ds_bpermute_b32 v241, v244, v241
	ds_bpermute_b32 v242, v244, v242
	ds_bpermute_b32 v243, v244, v243
	s_waitcnt lgkmcnt(4)
	global_store_dwordx4 v[140:141], v[236:239], off
	v_pk_mul_f32 v[136:137], v[174:175], v[186:187] op_sel_hi:[0,1]
	v_pk_mul_f32 v[132:133], v[174:175], v[180:181] op_sel_hi:[0,1]
	v_pk_mul_f32 v[134:135], v[174:175], v[182:183] op_sel_hi:[0,1]
	v_pk_mul_f32 v[142:143], v[20:21], v[138:139]
	v_pk_mul_f32 v[144:145], v[22:23], v[136:137]
	v_mad_i64_i32 v[206:207], s[34:35], v168, s36, v[176:177]
	v_pk_fma_f32 v[144:145], v[30:31], v[134:135], v[144:145] neg_lo:[0,0,1] neg_hi:[0,0,1]
	v_pk_fma_f32 v[142:143], v[28:29], v[132:133], v[142:143] neg_lo:[0,0,1] neg_hi:[0,0,1]
	v_pk_mul_f32 v[146:147], v[28:29], v[138:139]
	v_pk_mul_f32 v[180:181], v[30:31], v[136:137]
	v_lshl_add_u64 v[206:207], v[206:207], 0, v[178:179]
	v_pk_fma_f32 v[180:181], v[22:23], v[134:135], v[180:181]
	v_pk_fma_f32 v[146:147], v[20:21], v[132:133], v[146:147]
	v_cvt_pk_bf16_f32 v142, v142, v143
	v_cvt_pk_bf16_f32 v143, v144, v145
	s_nop 0
	v_cvt_pk_bf16_f32 v144, v146, v147
	v_cvt_pk_bf16_f32 v145, v180, v181
	v_mov_b32_e32 v228, v142
	v_mov_b32_e32 v229, v143
	v_mov_b32_e32 v230, v144
	v_mov_b32_e32 v231, v145
	s_nop 1
	v_permlane16_swap_b32_e32 v228, v230
	v_permlane16_swap_b32_e32 v229, v231
	ds_bpermute_b32 v228, v244, v228
	ds_bpermute_b32 v229, v244, v229
	ds_bpermute_b32 v230, v244, v230
	ds_bpermute_b32 v231, v244, v231
	s_waitcnt lgkmcnt(4)
	global_store_dwordx4 v[140:141], v[240:243], off offset:256
	v_pk_mul_f32 v[142:143], v[24:25], v[138:139]
	v_pk_mul_f32 v[144:145], v[26:27], v[136:137]
	v_pk_mul_f32 v[138:139], v[32:33], v[138:139]
	v_pk_mul_f32 v[136:137], v[34:35], v[136:137]
	v_pk_fma_f32 v[144:145], v[34:35], v[134:135], v[144:145] neg_lo:[0,0,1] neg_hi:[0,0,1]
	v_pk_fma_f32 v[142:143], v[32:33], v[132:133], v[142:143] neg_lo:[0,0,1] neg_hi:[0,0,1]
	v_pk_fma_f32 v[134:135], v[26:27], v[134:135], v[136:137]
	v_pk_fma_f32 v[132:133], v[24:25], v[132:133], v[138:139]
	v_cvt_pk_bf16_f32 v136, v142, v143
	v_cvt_pk_bf16_f32 v137, v144, v145
	v_pk_mul_f32 v[138:139], v[174:175], v[218:219] op_sel_hi:[0,1]
	v_cvt_pk_bf16_f32 v132, v132, v133
	v_cvt_pk_bf16_f32 v133, v134, v135
	v_mov_b32_e32 v232, v136
	v_mov_b32_e32 v233, v137
	v_mov_b32_e32 v234, v132
	v_mov_b32_e32 v235, v133
	s_nop 1
	v_permlane16_swap_b32_e32 v232, v234
	v_permlane16_swap_b32_e32 v233, v235
	ds_bpermute_b32 v232, v244, v232
	ds_bpermute_b32 v233, v244, v233
	ds_bpermute_b32 v234, v244, v234
	ds_bpermute_b32 v235, v244, v235
	s_waitcnt lgkmcnt(4)
	global_store_dwordx4 v[206:207], v[228:231], off
	v_pk_mul_f32 v[136:137], v[174:175], v[220:221] op_sel_hi:[0,1]
	v_pk_mul_f32 v[132:133], v[174:175], v[188:189] op_sel_hi:[0,1]
	v_pk_mul_f32 v[134:135], v[174:175], v[190:191] op_sel_hi:[0,1]
	v_pk_mul_f32 v[142:143], v[4:5], v[138:139]
	v_pk_mul_f32 v[144:145], v[6:7], v[136:137]
	v_mad_i64_i32 v[140:141], s[34:35], v166, s36, v[176:177]
	v_pk_fma_f32 v[144:145], v[14:15], v[134:135], v[144:145] neg_lo:[0,0,1] neg_hi:[0,0,1]
	v_pk_fma_f32 v[142:143], v[12:13], v[132:133], v[142:143] neg_lo:[0,0,1] neg_hi:[0,0,1]
	v_pk_mul_f32 v[146:147], v[12:13], v[138:139]
	v_pk_mul_f32 v[176:177], v[14:15], v[136:137]
	v_lshl_add_u64 v[140:141], v[140:141], 0, v[178:179]
	v_pk_fma_f32 v[176:177], v[6:7], v[134:135], v[176:177]
	v_pk_fma_f32 v[146:147], v[4:5], v[132:133], v[146:147]
	v_cvt_pk_bf16_f32 v142, v142, v143
	v_cvt_pk_bf16_f32 v143, v144, v145
	s_mov_b64 s[34:35], 0
	v_cvt_pk_bf16_f32 v144, v146, v147
	v_cvt_pk_bf16_f32 v145, v176, v177
	v_mov_b32_e32 v236, v142
	v_mov_b32_e32 v237, v143
	v_mov_b32_e32 v238, v144
	v_mov_b32_e32 v239, v145
	s_nop 1
	v_permlane16_swap_b32_e32 v236, v238
	v_permlane16_swap_b32_e32 v237, v239
	ds_bpermute_b32 v236, v244, v236
	ds_bpermute_b32 v237, v244, v237
	ds_bpermute_b32 v238, v244, v238
	ds_bpermute_b32 v239, v244, v239
	s_waitcnt lgkmcnt(4)
	global_store_dwordx4 v[206:207], v[232:235], off offset:256
	v_pk_mul_f32 v[142:143], v[8:9], v[138:139]
	v_pk_mul_f32 v[144:145], v[10:11], v[136:137]
	v_pk_mul_f32 v[138:139], v[16:17], v[138:139]
	v_pk_mul_f32 v[136:137], v[18:19], v[136:137]
	v_pk_fma_f32 v[144:145], v[18:19], v[134:135], v[144:145] neg_lo:[0,0,1] neg_hi:[0,0,1]
	v_pk_fma_f32 v[142:143], v[16:17], v[132:133], v[142:143] neg_lo:[0,0,1] neg_hi:[0,0,1]
	v_pk_fma_f32 v[134:135], v[10:11], v[134:135], v[136:137]
	v_pk_fma_f32 v[132:133], v[8:9], v[132:133], v[138:139]
	v_cvt_pk_bf16_f32 v136, v142, v143
	v_cvt_pk_bf16_f32 v137, v144, v145
	s_nop 0
	v_cvt_pk_bf16_f32 v132, v132, v133
	v_cvt_pk_bf16_f32 v133, v134, v135
	v_mov_b32_e32 v240, v136
	v_mov_b32_e32 v241, v137
	v_mov_b32_e32 v242, v132
	v_mov_b32_e32 v243, v133
	s_nop 1
	v_permlane16_swap_b32_e32 v240, v242
	v_permlane16_swap_b32_e32 v241, v243
	ds_bpermute_b32 v240, v244, v240
	ds_bpermute_b32 v241, v244, v241
	ds_bpermute_b32 v242, v244, v242
	ds_bpermute_b32 v243, v244, v243
	s_waitcnt lgkmcnt(4)
	global_store_dwordx4 v[140:141], v[236:239], off
	s_waitcnt lgkmcnt(0)
	global_store_dwordx4 v[140:141], v[240:243], off offset:256
